# P9 prologue: w_router fragment loads issued in 4 batches of 32 with one wait each instead of 64 serial 2-load round trips
# baseline (speedup 1.0000x reference)
.LBB0_793:
	s_or_b64 exec, exec, s[4:5]
	v_bfe_u32 v133, v1, 4, 2
	s_ashr_i32 s4, s0, 6
	v_lshlrev_b32_e32 v2, 3, v133
	v_lshl_or_b32 v114, s4, 8, v2
	v_ashrrev_i32_e32 v115, 31, v114
	v_and_b32_e32 v132, 15, v1
	v_and_b32_e32 v1, 31, v1
	v_lshlrev_b64 v[2:3], 7, v[114:115]
	v_lshlrev_b32_e32 v4, 2, v1
	s_waitcnt lgkmcnt(0)
	v_lshl_add_u64 v[2:3], s[10:11], 0, v[2:3]
	v_lshlrev_b32_e32 v130, 2, v132
	v_mov_b32_e32 v131, 0
	s_barrier
	v_lshl_add_u64 v[134:135], v[2:3], 0, v[130:131]
	global_load_dword v200, v4, s[6:7]
	s_add_i32 s3, s74, 0x3ff
	s_lshl_b32 s0, s90, 4
	s_add_u32 s16, s14, 0x2a000000
	s_addc_u32 s17, s15, 0
	s_abs_i32 s1, s74
	s_sub_i32 s6, 0, s1
	s_ashr_i32 s2, s3, 31
	s_ashr_i32 s5, s74, 31
	s_abs_i32 s3, s3
	v_cvt_f32_u32_e32 v136, s1
	v_rcp_iflag_f32_e32 v136, v136
	s_nop 0
	v_mul_f32_e32 v136, 0x4f7ffffe, v136
	v_cvt_u32_f32_e32 v136, v136
	s_nop 0
	v_readfirstlane_b32 s7, v136
	s_mul_i32 s6, s6, s7
	s_mul_hi_u32 s6, s7, s6
	s_add_i32 s7, s7, s6
	v_mov_b32_e32 v136, 0x1000
	v_mov_b32_e32 v137, 0
	global_load_dword v138, v[134:135], off
	global_load_dword v139, v[134:135], off offset:128
	global_load_dword v140, v[134:135], off offset:256
	global_load_dword v141, v[134:135], off offset:384
	global_load_dword v142, v[134:135], off offset:512
	global_load_dword v143, v[134:135], off offset:640
	global_load_dword v144, v[134:135], off offset:768
	global_load_dword v145, v[134:135], off offset:896
	global_load_dword v146, v[134:135], off offset:64
	global_load_dword v147, v[134:135], off offset:192
	global_load_dword v148, v[134:135], off offset:320
	global_load_dword v149, v[134:135], off offset:448
	global_load_dword v150, v[134:135], off offset:576
	global_load_dword v151, v[134:135], off offset:704
	global_load_dword v152, v[134:135], off offset:832
	global_load_dword v153, v[134:135], off offset:960
	v_lshl_add_u64 v[134:135], v[134:135], 0, v[136:137]
	global_load_dword v154, v[134:135], off
	global_load_dword v155, v[134:135], off offset:128
	global_load_dword v156, v[134:135], off offset:256
	global_load_dword v157, v[134:135], off offset:384
	global_load_dword v158, v[134:135], off offset:512
	global_load_dword v159, v[134:135], off offset:640
	global_load_dword v160, v[134:135], off offset:768
	global_load_dword v161, v[134:135], off offset:896
	global_load_dword v162, v[134:135], off offset:64
	global_load_dword v163, v[134:135], off offset:192
	global_load_dword v164, v[134:135], off offset:320
	global_load_dword v165, v[134:135], off offset:448
	global_load_dword v166, v[134:135], off offset:576
	global_load_dword v167, v[134:135], off offset:704
	global_load_dword v168, v[134:135], off offset:832
	global_load_dword v169, v[134:135], off offset:960
	v_lshl_add_u64 v[134:135], v[134:135], 0, v[136:137]
	s_waitcnt vmcnt(0)
	v_cvt_pk_bf16_f32 v2, v138, v139
	s_nop 0
	v_and_b32_e32 v170, 0xffff0000, v2
	v_lshlrev_b32_e32 v171, 16, v2
	v_sub_f32_e32 v139, v139, v170
	v_sub_f32_e32 v138, v138, v171
	v_cvt_pk_bf16_f32 v6, v138, v139
	v_cvt_pk_bf16_f32 v3, v140, v141
	s_nop 0
	v_and_b32_e32 v170, 0xffff0000, v3
	v_lshlrev_b32_e32 v171, 16, v3
	v_sub_f32_e32 v141, v141, v170
	v_sub_f32_e32 v140, v140, v171
	v_cvt_pk_bf16_f32 v7, v140, v141
	v_cvt_pk_bf16_f32 v4, v142, v143
	s_nop 0
	v_and_b32_e32 v170, 0xffff0000, v4
	v_lshlrev_b32_e32 v171, 16, v4
	v_sub_f32_e32 v143, v143, v170
	v_sub_f32_e32 v142, v142, v171
	v_cvt_pk_bf16_f32 v8, v142, v143
	v_cvt_pk_bf16_f32 v5, v144, v145
	s_nop 0
	v_and_b32_e32 v170, 0xffff0000, v5
	v_lshlrev_b32_e32 v171, 16, v5
	v_sub_f32_e32 v145, v145, v170
	v_sub_f32_e32 v144, v144, v171
	v_cvt_pk_bf16_f32 v9, v144, v145
	v_cvt_pk_bf16_f32 v10, v146, v147
	s_nop 0
	v_and_b32_e32 v170, 0xffff0000, v10
	v_lshlrev_b32_e32 v171, 16, v10
	v_sub_f32_e32 v147, v147, v170
	v_sub_f32_e32 v146, v146, v171
	v_cvt_pk_bf16_f32 v14, v146, v147
	v_cvt_pk_bf16_f32 v11, v148, v149
	s_nop 0
	v_and_b32_e32 v170, 0xffff0000, v11
	v_lshlrev_b32_e32 v171, 16, v11
	v_sub_f32_e32 v149, v149, v170
	v_sub_f32_e32 v148, v148, v171
	v_cvt_pk_bf16_f32 v15, v148, v149
	v_cvt_pk_bf16_f32 v12, v150, v151
	s_nop 0
	v_and_b32_e32 v170, 0xffff0000, v12
	v_lshlrev_b32_e32 v171, 16, v12
	v_sub_f32_e32 v151, v151, v170
	v_sub_f32_e32 v150, v150, v171
	v_cvt_pk_bf16_f32 v16, v150, v151
	v_cvt_pk_bf16_f32 v13, v152, v153
	s_nop 0
	v_and_b32_e32 v170, 0xffff0000, v13
	v_lshlrev_b32_e32 v171, 16, v13
	v_sub_f32_e32 v153, v153, v170
	v_sub_f32_e32 v152, v152, v171
	v_cvt_pk_bf16_f32 v17, v152, v153
	v_cvt_pk_bf16_f32 v18, v154, v155
	s_nop 0
	v_and_b32_e32 v170, 0xffff0000, v18
	v_lshlrev_b32_e32 v171, 16, v18
	v_sub_f32_e32 v155, v155, v170
	v_sub_f32_e32 v154, v154, v171
	v_cvt_pk_bf16_f32 v22, v154, v155
	v_cvt_pk_bf16_f32 v19, v156, v157
	s_nop 0
	v_and_b32_e32 v170, 0xffff0000, v19
	v_lshlrev_b32_e32 v171, 16, v19
	v_sub_f32_e32 v157, v157, v170
	v_sub_f32_e32 v156, v156, v171
	v_cvt_pk_bf16_f32 v23, v156, v157
	v_cvt_pk_bf16_f32 v20, v158, v159
	s_nop 0
	v_and_b32_e32 v170, 0xffff0000, v20
	v_lshlrev_b32_e32 v171, 16, v20
	v_sub_f32_e32 v159, v159, v170
	v_sub_f32_e32 v158, v158, v171
	v_cvt_pk_bf16_f32 v24, v158, v159
	v_cvt_pk_bf16_f32 v21, v160, v161
	s_nop 0
	v_and_b32_e32 v170, 0xffff0000, v21
	v_lshlrev_b32_e32 v171, 16, v21
	v_sub_f32_e32 v161, v161, v170
	v_sub_f32_e32 v160, v160, v171
	v_cvt_pk_bf16_f32 v25, v160, v161
	v_cvt_pk_bf16_f32 v26, v162, v163
	s_nop 0
	v_and_b32_e32 v170, 0xffff0000, v26
	v_lshlrev_b32_e32 v171, 16, v26
	v_sub_f32_e32 v163, v163, v170
	v_sub_f32_e32 v162, v162, v171
	v_cvt_pk_bf16_f32 v30, v162, v163
	v_cvt_pk_bf16_f32 v27, v164, v165
	s_nop 0
	v_and_b32_e32 v170, 0xffff0000, v27
	v_lshlrev_b32_e32 v171, 16, v27
	v_sub_f32_e32 v165, v165, v170
	v_sub_f32_e32 v164, v164, v171
	v_cvt_pk_bf16_f32 v31, v164, v165
	v_cvt_pk_bf16_f32 v28, v166, v167
	s_nop 0
	v_and_b32_e32 v170, 0xffff0000, v28
	v_lshlrev_b32_e32 v171, 16, v28
	v_sub_f32_e32 v167, v167, v170
	v_sub_f32_e32 v166, v166, v171
	v_cvt_pk_bf16_f32 v32, v166, v167
	v_cvt_pk_bf16_f32 v29, v168, v169
	s_nop 0
	v_and_b32_e32 v170, 0xffff0000, v29
	v_lshlrev_b32_e32 v171, 16, v29
	v_sub_f32_e32 v169, v169, v170
	v_sub_f32_e32 v168, v168, v171
	v_cvt_pk_bf16_f32 v33, v168, v169
	global_load_dword v138, v[134:135], off
	global_load_dword v139, v[134:135], off offset:128
	global_load_dword v140, v[134:135], off offset:256
	global_load_dword v141, v[134:135], off offset:384
	global_load_dword v142, v[134:135], off offset:512
	global_load_dword v143, v[134:135], off offset:640
	global_load_dword v144, v[134:135], off offset:768
	global_load_dword v145, v[134:135], off offset:896
	global_load_dword v146, v[134:135], off offset:64
	global_load_dword v147, v[134:135], off offset:192
	global_load_dword v148, v[134:135], off offset:320
	global_load_dword v149, v[134:135], off offset:448
	global_load_dword v150, v[134:135], off offset:576
	global_load_dword v151, v[134:135], off offset:704
	global_load_dword v152, v[134:135], off offset:832
	global_load_dword v153, v[134:135], off offset:960
	v_lshl_add_u64 v[134:135], v[134:135], 0, v[136:137]
	global_load_dword v154, v[134:135], off
	global_load_dword v155, v[134:135], off offset:128
	global_load_dword v156, v[134:135], off offset:256
	global_load_dword v157, v[134:135], off offset:384
	global_load_dword v158, v[134:135], off offset:512
	global_load_dword v159, v[134:135], off offset:640
	global_load_dword v160, v[134:135], off offset:768
	global_load_dword v161, v[134:135], off offset:896
	global_load_dword v162, v[134:135], off offset:64
	global_load_dword v163, v[134:135], off offset:192
	global_load_dword v164, v[134:135], off offset:320
	global_load_dword v165, v[134:135], off offset:448
	global_load_dword v166, v[134:135], off offset:576
	global_load_dword v167, v[134:135], off offset:704
	global_load_dword v168, v[134:135], off offset:832
	global_load_dword v169, v[134:135], off offset:960
	v_lshl_add_u64 v[134:135], v[134:135], 0, v[136:137]
	s_waitcnt vmcnt(0)
	v_cvt_pk_bf16_f32 v34, v138, v139
	s_nop 0
	v_and_b32_e32 v170, 0xffff0000, v34
	v_lshlrev_b32_e32 v171, 16, v34
	v_sub_f32_e32 v139, v139, v170
	v_sub_f32_e32 v138, v138, v171
	v_cvt_pk_bf16_f32 v38, v138, v139
	v_cvt_pk_bf16_f32 v35, v140, v141
	s_nop 0
	v_and_b32_e32 v170, 0xffff0000, v35
	v_lshlrev_b32_e32 v171, 16, v35
	v_sub_f32_e32 v141, v141, v170
	v_sub_f32_e32 v140, v140, v171
	v_cvt_pk_bf16_f32 v39, v140, v141
	v_cvt_pk_bf16_f32 v36, v142, v143
	s_nop 0
	v_and_b32_e32 v170, 0xffff0000, v36
	v_lshlrev_b32_e32 v171, 16, v36
	v_sub_f32_e32 v143, v143, v170
	v_sub_f32_e32 v142, v142, v171
	v_cvt_pk_bf16_f32 v40, v142, v143
	v_cvt_pk_bf16_f32 v37, v144, v145
	s_nop 0
	v_and_b32_e32 v170, 0xffff0000, v37
	v_lshlrev_b32_e32 v171, 16, v37
	v_sub_f32_e32 v145, v145, v170
	v_sub_f32_e32 v144, v144, v171
	v_cvt_pk_bf16_f32 v41, v144, v145
	v_cvt_pk_bf16_f32 v42, v146, v147
	s_nop 0
	v_and_b32_e32 v170, 0xffff0000, v42
	v_lshlrev_b32_e32 v171, 16, v42
	v_sub_f32_e32 v147, v147, v170
	v_sub_f32_e32 v146, v146, v171
	v_cvt_pk_bf16_f32 v46, v146, v147
	v_cvt_pk_bf16_f32 v43, v148, v149
	s_nop 0
	v_and_b32_e32 v170, 0xffff0000, v43
	v_lshlrev_b32_e32 v171, 16, v43
	v_sub_f32_e32 v149, v149, v170
	v_sub_f32_e32 v148, v148, v171
	v_cvt_pk_bf16_f32 v47, v148, v149
	v_cvt_pk_bf16_f32 v44, v150, v151
	s_nop 0
	v_and_b32_e32 v170, 0xffff0000, v44
	v_lshlrev_b32_e32 v171, 16, v44
	v_sub_f32_e32 v151, v151, v170
	v_sub_f32_e32 v150, v150, v171
	v_cvt_pk_bf16_f32 v48, v150, v151
	v_cvt_pk_bf16_f32 v45, v152, v153
	s_nop 0
	v_and_b32_e32 v170, 0xffff0000, v45
	v_lshlrev_b32_e32 v171, 16, v45
	v_sub_f32_e32 v153, v153, v170
	v_sub_f32_e32 v152, v152, v171
	v_cvt_pk_bf16_f32 v49, v152, v153
	v_cvt_pk_bf16_f32 v50, v154, v155
	s_nop 0
	v_and_b32_e32 v170, 0xffff0000, v50
	v_lshlrev_b32_e32 v171, 16, v50
	v_sub_f32_e32 v155, v155, v170
	v_sub_f32_e32 v154, v154, v171
	v_cvt_pk_bf16_f32 v54, v154, v155
	v_cvt_pk_bf16_f32 v51, v156, v157
	s_nop 0
	v_and_b32_e32 v170, 0xffff0000, v51
	v_lshlrev_b32_e32 v171, 16, v51
	v_sub_f32_e32 v157, v157, v170
	v_sub_f32_e32 v156, v156, v171
	v_cvt_pk_bf16_f32 v55, v156, v157
	v_cvt_pk_bf16_f32 v52, v158, v159
	s_nop 0
	v_and_b32_e32 v170, 0xffff0000, v52
	v_lshlrev_b32_e32 v171, 16, v52
	v_sub_f32_e32 v159, v159, v170
	v_sub_f32_e32 v158, v158, v171
	v_cvt_pk_bf16_f32 v56, v158, v159
	v_cvt_pk_bf16_f32 v53, v160, v161
	s_nop 0
	v_and_b32_e32 v170, 0xffff0000, v53
	v_lshlrev_b32_e32 v171, 16, v53
	v_sub_f32_e32 v161, v161, v170
	v_sub_f32_e32 v160, v160, v171
	v_cvt_pk_bf16_f32 v57, v160, v161
	v_cvt_pk_bf16_f32 v58, v162, v163
	s_nop 0
	v_and_b32_e32 v170, 0xffff0000, v58
	v_lshlrev_b32_e32 v171, 16, v58
	v_sub_f32_e32 v163, v163, v170
	v_sub_f32_e32 v162, v162, v171
	v_cvt_pk_bf16_f32 v62, v162, v163
	v_cvt_pk_bf16_f32 v59, v164, v165
	s_nop 0
	v_and_b32_e32 v170, 0xffff0000, v59
	v_lshlrev_b32_e32 v171, 16, v59
	v_sub_f32_e32 v165, v165, v170
	v_sub_f32_e32 v164, v164, v171
	v_cvt_pk_bf16_f32 v63, v164, v165
	v_cvt_pk_bf16_f32 v60, v166, v167
	s_nop 0
	v_and_b32_e32 v170, 0xffff0000, v60
	v_lshlrev_b32_e32 v171, 16, v60
	v_sub_f32_e32 v167, v167, v170
	v_sub_f32_e32 v166, v166, v171
	v_cvt_pk_bf16_f32 v64, v166, v167
	v_cvt_pk_bf16_f32 v61, v168, v169
	s_nop 0
	v_and_b32_e32 v170, 0xffff0000, v61
	v_lshlrev_b32_e32 v171, 16, v61
	v_sub_f32_e32 v169, v169, v170
	v_sub_f32_e32 v168, v168, v171
	v_cvt_pk_bf16_f32 v65, v168, v169
	global_load_dword v138, v[134:135], off
	global_load_dword v139, v[134:135], off offset:128
	global_load_dword v140, v[134:135], off offset:256
	global_load_dword v141, v[134:135], off offset:384
	global_load_dword v142, v[134:135], off offset:512
	global_load_dword v143, v[134:135], off offset:640
	global_load_dword v144, v[134:135], off offset:768
	global_load_dword v145, v[134:135], off offset:896
	global_load_dword v146, v[134:135], off offset:64
	global_load_dword v147, v[134:135], off offset:192
	global_load_dword v148, v[134:135], off offset:320
	global_load_dword v149, v[134:135], off offset:448
	global_load_dword v150, v[134:135], off offset:576
	global_load_dword v151, v[134:135], off offset:704
	global_load_dword v152, v[134:135], off offset:832
	global_load_dword v153, v[134:135], off offset:960
	v_lshl_add_u64 v[134:135], v[134:135], 0, v[136:137]
	global_load_dword v154, v[134:135], off
	global_load_dword v155, v[134:135], off offset:128
	global_load_dword v156, v[134:135], off offset:256
	global_load_dword v157, v[134:135], off offset:384
	global_load_dword v158, v[134:135], off offset:512
	global_load_dword v159, v[134:135], off offset:640
	global_load_dword v160, v[134:135], off offset:768
	global_load_dword v161, v[134:135], off offset:896
	global_load_dword v162, v[134:135], off offset:64
	global_load_dword v163, v[134:135], off offset:192
	global_load_dword v164, v[134:135], off offset:320
	global_load_dword v165, v[134:135], off offset:448
	global_load_dword v166, v[134:135], off offset:576
	global_load_dword v167, v[134:135], off offset:704
	global_load_dword v168, v[134:135], off offset:832
	global_load_dword v169, v[134:135], off offset:960
	v_lshl_add_u64 v[134:135], v[134:135], 0, v[136:137]
	s_waitcnt vmcnt(0)
	v_cvt_pk_bf16_f32 v66, v138, v139
	s_nop 0
	v_and_b32_e32 v170, 0xffff0000, v66
	v_lshlrev_b32_e32 v171, 16, v66
	v_sub_f32_e32 v139, v139, v170
	v_sub_f32_e32 v138, v138, v171
	v_cvt_pk_bf16_f32 v70, v138, v139
	v_cvt_pk_bf16_f32 v67, v140, v141
	s_nop 0
	v_and_b32_e32 v170, 0xffff0000, v67
	v_lshlrev_b32_e32 v171, 16, v67
	v_sub_f32_e32 v141, v141, v170
	v_sub_f32_e32 v140, v140, v171
	v_cvt_pk_bf16_f32 v71, v140, v141
	v_cvt_pk_bf16_f32 v68, v142, v143
	s_nop 0
	v_and_b32_e32 v170, 0xffff0000, v68
	v_lshlrev_b32_e32 v171, 16, v68
	v_sub_f32_e32 v143, v143, v170
	v_sub_f32_e32 v142, v142, v171
	v_cvt_pk_bf16_f32 v72, v142, v143
	v_cvt_pk_bf16_f32 v69, v144, v145
	s_nop 0
	v_and_b32_e32 v170, 0xffff0000, v69
	v_lshlrev_b32_e32 v171, 16, v69
	v_sub_f32_e32 v145, v145, v170
	v_sub_f32_e32 v144, v144, v171
	v_cvt_pk_bf16_f32 v73, v144, v145
	v_cvt_pk_bf16_f32 v74, v146, v147
	s_nop 0
	v_and_b32_e32 v170, 0xffff0000, v74
	v_lshlrev_b32_e32 v171, 16, v74
	v_sub_f32_e32 v147, v147, v170
	v_sub_f32_e32 v146, v146, v171
	v_cvt_pk_bf16_f32 v78, v146, v147
	v_cvt_pk_bf16_f32 v75, v148, v149
	s_nop 0
	v_and_b32_e32 v170, 0xffff0000, v75
	v_lshlrev_b32_e32 v171, 16, v75
	v_sub_f32_e32 v149, v149, v170
	v_sub_f32_e32 v148, v148, v171
	v_cvt_pk_bf16_f32 v79, v148, v149
	v_cvt_pk_bf16_f32 v76, v150, v151
	s_nop 0
	v_and_b32_e32 v170, 0xffff0000, v76
	v_lshlrev_b32_e32 v171, 16, v76
	v_sub_f32_e32 v151, v151, v170
	v_sub_f32_e32 v150, v150, v171
	v_cvt_pk_bf16_f32 v80, v150, v151
	v_cvt_pk_bf16_f32 v77, v152, v153
	s_nop 0
	v_and_b32_e32 v170, 0xffff0000, v77
	v_lshlrev_b32_e32 v171, 16, v77
	v_sub_f32_e32 v153, v153, v170
	v_sub_f32_e32 v152, v152, v171
	v_cvt_pk_bf16_f32 v81, v152, v153
	v_cvt_pk_bf16_f32 v82, v154, v155
	s_nop 0
	v_and_b32_e32 v170, 0xffff0000, v82
	v_lshlrev_b32_e32 v171, 16, v82
	v_sub_f32_e32 v155, v155, v170
	v_sub_f32_e32 v154, v154, v171
	v_cvt_pk_bf16_f32 v86, v154, v155
	v_cvt_pk_bf16_f32 v83, v156, v157
	s_nop 0
	v_and_b32_e32 v170, 0xffff0000, v83
	v_lshlrev_b32_e32 v171, 16, v83
	v_sub_f32_e32 v157, v157, v170
	v_sub_f32_e32 v156, v156, v171
	v_cvt_pk_bf16_f32 v87, v156, v157
	v_cvt_pk_bf16_f32 v84, v158, v159
	s_nop 0
	v_and_b32_e32 v170, 0xffff0000, v84
	v_lshlrev_b32_e32 v171, 16, v84
	v_sub_f32_e32 v159, v159, v170
	v_sub_f32_e32 v158, v158, v171
	v_cvt_pk_bf16_f32 v88, v158, v159
	v_cvt_pk_bf16_f32 v85, v160, v161
	s_nop 0
	v_and_b32_e32 v170, 0xffff0000, v85
	v_lshlrev_b32_e32 v171, 16, v85
	v_sub_f32_e32 v161, v161, v170
	v_sub_f32_e32 v160, v160, v171
	v_cvt_pk_bf16_f32 v89, v160, v161
	v_cvt_pk_bf16_f32 v90, v162, v163
	s_nop 0
	v_and_b32_e32 v170, 0xffff0000, v90
	v_lshlrev_b32_e32 v171, 16, v90
	v_sub_f32_e32 v163, v163, v170
	v_sub_f32_e32 v162, v162, v171
	v_cvt_pk_bf16_f32 v94, v162, v163
	v_cvt_pk_bf16_f32 v91, v164, v165
	s_nop 0
	v_and_b32_e32 v170, 0xffff0000, v91
	v_lshlrev_b32_e32 v171, 16, v91
	v_sub_f32_e32 v165, v165, v170
	v_sub_f32_e32 v164, v164, v171
	v_cvt_pk_bf16_f32 v95, v164, v165
	v_cvt_pk_bf16_f32 v92, v166, v167
	s_nop 0
	v_and_b32_e32 v170, 0xffff0000, v92
	v_lshlrev_b32_e32 v171, 16, v92
	v_sub_f32_e32 v167, v167, v170
	v_sub_f32_e32 v166, v166, v171
	v_cvt_pk_bf16_f32 v96, v166, v167
	v_cvt_pk_bf16_f32 v93, v168, v169
	s_nop 0
	v_and_b32_e32 v170, 0xffff0000, v93
	v_lshlrev_b32_e32 v171, 16, v93
	v_sub_f32_e32 v169, v169, v170
	v_sub_f32_e32 v168, v168, v171
	v_cvt_pk_bf16_f32 v97, v168, v169
	global_load_dword v138, v[134:135], off
	global_load_dword v139, v[134:135], off offset:128
	global_load_dword v140, v[134:135], off offset:256
	global_load_dword v141, v[134:135], off offset:384
	global_load_dword v142, v[134:135], off offset:512
	global_load_dword v143, v[134:135], off offset:640
	global_load_dword v144, v[134:135], off offset:768
	global_load_dword v145, v[134:135], off offset:896
	global_load_dword v146, v[134:135], off offset:64
	global_load_dword v147, v[134:135], off offset:192
	global_load_dword v148, v[134:135], off offset:320
	global_load_dword v149, v[134:135], off offset:448
	global_load_dword v150, v[134:135], off offset:576
	global_load_dword v151, v[134:135], off offset:704
	global_load_dword v152, v[134:135], off offset:832
	global_load_dword v153, v[134:135], off offset:960
	v_lshl_add_u64 v[134:135], v[134:135], 0, v[136:137]
	global_load_dword v154, v[134:135], off
	global_load_dword v155, v[134:135], off offset:128
	global_load_dword v156, v[134:135], off offset:256
	global_load_dword v157, v[134:135], off offset:384
	global_load_dword v158, v[134:135], off offset:512
	global_load_dword v159, v[134:135], off offset:640
	global_load_dword v160, v[134:135], off offset:768
	global_load_dword v161, v[134:135], off offset:896
	global_load_dword v162, v[134:135], off offset:64
	global_load_dword v163, v[134:135], off offset:192
	global_load_dword v164, v[134:135], off offset:320
	global_load_dword v165, v[134:135], off offset:448
	global_load_dword v166, v[134:135], off offset:576
	global_load_dword v167, v[134:135], off offset:704
	global_load_dword v168, v[134:135], off offset:832
	global_load_dword v169, v[134:135], off offset:960
	v_lshl_add_u64 v[134:135], v[134:135], 0, v[136:137]
	s_waitcnt vmcnt(0)
	v_cvt_pk_bf16_f32 v98, v138, v139
	s_nop 0
	v_and_b32_e32 v170, 0xffff0000, v98
	v_lshlrev_b32_e32 v171, 16, v98
	v_sub_f32_e32 v139, v139, v170
	v_sub_f32_e32 v138, v138, v171
	v_cvt_pk_bf16_f32 v102, v138, v139
	v_cvt_pk_bf16_f32 v99, v140, v141
	s_nop 0
	v_and_b32_e32 v170, 0xffff0000, v99
	v_lshlrev_b32_e32 v171, 16, v99
	v_sub_f32_e32 v141, v141, v170
	v_sub_f32_e32 v140, v140, v171
	v_cvt_pk_bf16_f32 v103, v140, v141
	v_cvt_pk_bf16_f32 v100, v142, v143
	s_nop 0
	v_and_b32_e32 v170, 0xffff0000, v100
	v_lshlrev_b32_e32 v171, 16, v100
	v_sub_f32_e32 v143, v143, v170
	v_sub_f32_e32 v142, v142, v171
	v_cvt_pk_bf16_f32 v104, v142, v143
	v_cvt_pk_bf16_f32 v101, v144, v145
	s_nop 0
	v_and_b32_e32 v170, 0xffff0000, v101
	v_lshlrev_b32_e32 v171, 16, v101
	v_sub_f32_e32 v145, v145, v170
	v_sub_f32_e32 v144, v144, v171
	v_cvt_pk_bf16_f32 v105, v144, v145
	v_cvt_pk_bf16_f32 v106, v146, v147
	s_nop 0
	v_and_b32_e32 v170, 0xffff0000, v106
	v_lshlrev_b32_e32 v171, 16, v106
	v_sub_f32_e32 v147, v147, v170
	v_sub_f32_e32 v146, v146, v171
	v_cvt_pk_bf16_f32 v110, v146, v147
	v_cvt_pk_bf16_f32 v107, v148, v149
	s_nop 0
	v_and_b32_e32 v170, 0xffff0000, v107
	v_lshlrev_b32_e32 v171, 16, v107
	v_sub_f32_e32 v149, v149, v170
	v_sub_f32_e32 v148, v148, v171
	v_cvt_pk_bf16_f32 v111, v148, v149
	v_cvt_pk_bf16_f32 v108, v150, v151
	s_nop 0
	v_and_b32_e32 v170, 0xffff0000, v108
	v_lshlrev_b32_e32 v171, 16, v108
	v_sub_f32_e32 v151, v151, v170
	v_sub_f32_e32 v150, v150, v171
	v_cvt_pk_bf16_f32 v112, v150, v151
	v_cvt_pk_bf16_f32 v109, v152, v153
	s_nop 0
	v_and_b32_e32 v170, 0xffff0000, v109
	v_lshlrev_b32_e32 v171, 16, v109
	v_sub_f32_e32 v153, v153, v170
	v_sub_f32_e32 v152, v152, v171
	v_cvt_pk_bf16_f32 v113, v152, v153
	v_cvt_pk_bf16_f32 v114, v154, v155
	s_nop 0
	v_and_b32_e32 v170, 0xffff0000, v114
	v_lshlrev_b32_e32 v171, 16, v114
	v_sub_f32_e32 v155, v155, v170
	v_sub_f32_e32 v154, v154, v171
	v_cvt_pk_bf16_f32 v118, v154, v155
	v_cvt_pk_bf16_f32 v115, v156, v157
	s_nop 0
	v_and_b32_e32 v170, 0xffff0000, v115
	v_lshlrev_b32_e32 v171, 16, v115
	v_sub_f32_e32 v157, v157, v170
	v_sub_f32_e32 v156, v156, v171
	v_cvt_pk_bf16_f32 v119, v156, v157
	v_cvt_pk_bf16_f32 v116, v158, v159
	s_nop 0
	v_and_b32_e32 v170, 0xffff0000, v116
	v_lshlrev_b32_e32 v171, 16, v116
	v_sub_f32_e32 v159, v159, v170
	v_sub_f32_e32 v158, v158, v171
	v_cvt_pk_bf16_f32 v120, v158, v159
	v_cvt_pk_bf16_f32 v117, v160, v161
	s_nop 0
	v_and_b32_e32 v170, 0xffff0000, v117
	v_lshlrev_b32_e32 v171, 16, v117
	v_sub_f32_e32 v161, v161, v170
	v_sub_f32_e32 v160, v160, v171
	v_cvt_pk_bf16_f32 v121, v160, v161
	v_cvt_pk_bf16_f32 v122, v162, v163
	s_nop 0
	v_and_b32_e32 v170, 0xffff0000, v122
	v_lshlrev_b32_e32 v171, 16, v122
	v_sub_f32_e32 v163, v163, v170
	v_sub_f32_e32 v162, v162, v171
	v_cvt_pk_bf16_f32 v126, v162, v163
	v_cvt_pk_bf16_f32 v123, v164, v165
	s_nop 0
	v_and_b32_e32 v170, 0xffff0000, v123
	v_lshlrev_b32_e32 v171, 16, v123
	v_sub_f32_e32 v165, v165, v170
	v_sub_f32_e32 v164, v164, v171
	v_cvt_pk_bf16_f32 v127, v164, v165
	v_cvt_pk_bf16_f32 v124, v166, v167
	s_nop 0
	v_and_b32_e32 v170, 0xffff0000, v124
	v_lshlrev_b32_e32 v171, 16, v124
	v_sub_f32_e32 v167, v167, v170
	v_sub_f32_e32 v166, v166, v171
	v_cvt_pk_bf16_f32 v128, v166, v167
	v_cvt_pk_bf16_f32 v125, v168, v169
	s_nop 0
	v_and_b32_e32 v170, 0xffff0000, v125
	v_lshlrev_b32_e32 v171, 16, v125
	v_sub_f32_e32 v169, v169, v170
	v_sub_f32_e32 v168, v168, v171
	v_cvt_pk_bf16_f32 v129, v168, v169
	s_cmpk_lt_i32 s90, 0x400
	s_mul_hi_u32 s6, s3, s7
	s_cbranch_scc0 .LBB0_795
	s_lshl_b32 s7, s4, 1
	v_mov_b32_e32 v130, v0
	s_add_i32 s8, s7, s0
	s_ashr_i32 s9, s8, 31
	v_and_b32_e32 v130, 63, v130
	s_lshl_b64 s[10:11], s[8:9], 12
	s_or_b32 s8, s8, 1
	v_lshlrev_b32_e32 v130, 3, v130
	s_ashr_i32 s9, s8, 31
	v_lshl_add_u64 v[130:131], s[16:17], 0, v[130:131]
	s_lshl_b64 s[8:9], s[8:9], 12
	v_lshl_add_u64 v[134:135], v[130:131], 0, s[10:11]
	v_lshl_add_u64 v[130:131], v[130:131], 0, s[8:9]
	global_load_dwordx2 v[138:139], v[134:135], off
	global_load_dwordx2 v[140:141], v[134:135], off offset:512
	global_load_dwordx2 v[142:143], v[134:135], off offset:1024
	global_load_dwordx2 v[144:145], v[134:135], off offset:1536
	global_load_dwordx2 v[146:147], v[134:135], off offset:2048
	global_load_dwordx2 v[148:149], v[134:135], off offset:2560
	global_load_dwordx2 v[150:151], v[134:135], off offset:3072
	global_load_dwordx2 v[152:153], v[134:135], off offset:3584
	global_load_dwordx2 v[154:155], v[130:131], off
	global_load_dwordx2 v[156:157], v[130:131], off offset:512
	global_load_dwordx2 v[158:159], v[130:131], off offset:1024
	global_load_dwordx2 v[160:161], v[130:131], off offset:1536
	global_load_dwordx2 v[162:163], v[130:131], off offset:2048
	global_load_dwordx2 v[164:165], v[130:131], off offset:2560
	global_load_dwordx2 v[166:167], v[130:131], off offset:3072
	global_load_dwordx2 v[168:169], v[130:131], off offset:3584
